# K-loop header relaxed-wait flag: v_cndmask/v_readfirstlane/s_cmp/s_cselect chain replaced by one s_mov_b64 of the already-uniform scalar mask (5 GEMM loops)
# speedup vs baseline: 1.0007x; 1.0007x over previous
; #define PG8_STAGE_A(bufoff, gbase, VO, h) do { _Pragma("unroll") for (int _i = 0; _i < 2; ++_i) \
;         __builtin_amdgcn_global_load_lds((const unsigned*)((const char*)(gbase) + (VO)[h][_i]), (LAS unsigned*)(lds + (bufoff) + ldsw + _i * 8192), 16, 0, 0); } while (0)
; #define PG8_SCHED __builtin_amdgcn_sched_barrier(0)
;     ...
;             const bool last = (t == nt - 2); int rxi = (relax && t == 0) ? 1 : 0; asm volatile("" : "+v"(rxi)); const bool rx = __builtin_amdgcn_readfirstlane(rxi) != 0;
;             if constexpr (Epi::HAS_MID) { constexpr int SEGT = (F8 != 0) ? 8 : 16; if (t == SEGT || t == 2 * SEGT) { PG8_SCHED; E.mid(acc, cur, t / SEGT, wr, wc, fr, fq); PG8_SCHED; } }
;             const char* a1 = cA + (size_t)(t + 1) * kstep;
;             const char* a2 = last ? nA : cA + (size_t)(t + 2) * kstep; const char* b2 = last ? nB : cB + (size_t)(t + 2) * kstepB;
;             const char* a3 = a2 + kstep; const char* b3 = b2 + kstepB;
;             unsigned vo2[2][2];
; #pragma unroll
;             for (int h = 0; h < 2; ++h)
; #pragma unroll
;                 for (int i = 0; i < 2; ++i) vo2[h][i] = (GATHER && last) ? voffN[h][i] : voffA[h][i];
;             PG8_LDB(B0, 0, 0); PG8_LDB(B1, 0, 1); PG8_SCHED; PG8_LDA(At, 0, 0); if (!rx) PG8_STAGE_A(PG8_SA(1, 1), a1, voffA, 1);
.LBB0_372:
	s_cmp_eq_u32 s18, 0
	s_cselect_b64 s[2:3], -1, 0
	s_and_b64 s[2:3], s[14:15], s[2:3]
	s_mov_b64 s[24:25], s[2:3]
	s_nop 0
	v_add_u32_e32 v24, 0x10000, v218
	ds_read_b128 v[158:161], v24
	ds_read_b128 v[154:157], v24 offset:1024
	ds_read_b128 v[150:153], v24 offset:2048
	ds_read_b128 v[146:149], v24 offset:3072
	v_add_u32_e32 v24, 0x14000, v218
	ds_read_b128 v[44:47], v24
	ds_read_b128 v[40:43], v24 offset:1024
	ds_read_b128 v[28:31], v24 offset:2048
	ds_read_b128 v[24:27], v24 offset:3072
	ds_read_b128 v[186:189], v219
	ds_read_b128 v[190:193], v219 offset:1024
	ds_read_b128 v[178:181], v219 offset:2048
	ds_read_b128 v[182:185], v219 offset:3072
	ds_read_b128 v[170:173], v219 offset:4096
	ds_read_b128 v[174:177], v219 offset:5120
	ds_read_b128 v[166:169], v219 offset:6144
	ds_read_b128 v[162:165], v219 offset:7168
	s_and_b64 vcc, exec, s[24:25]
	s_cbranch_vccz .LBB0_380
	s_waitcnt vmcnt(24)
	s_cbranch_execnz .LBB0_375

; #define PG8_STAGE_A(bufoff, gbase, VO, h) do { _Pragma("unroll") for (int _i = 0; _i < 2; ++_i) \
;         __builtin_amdgcn_global_load_lds((const unsigned*)((const char*)(gbase) + (VO)[h][_i]), (LAS unsigned*)(lds + (bufoff) + ldsw + _i * 8192), 16, 0, 0); } while (0)
; #define PG8_SCHED __builtin_amdgcn_sched_barrier(0)
;     ...
;             const bool last = (t == nt - 2); int rxi = (relax && t == 0) ? 1 : 0; asm volatile("" : "+v"(rxi)); const bool rx = __builtin_amdgcn_readfirstlane(rxi) != 0;
;             if constexpr (Epi::HAS_MID) { constexpr int SEGT = (F8 != 0) ? 8 : 16; if (t == SEGT || t == 2 * SEGT) { PG8_SCHED; E.mid(acc, cur, t / SEGT, wr, wc, fr, fq); PG8_SCHED; } }
;             const char* a1 = cA + (size_t)(t + 1) * kstep;
;             const char* a2 = last ? nA : cA + (size_t)(t + 2) * kstep; const char* b2 = last ? nB : cB + (size_t)(t + 2) * kstepB;
;             const char* a3 = a2 + kstep; const char* b3 = b2 + kstepB;
;             unsigned vo2[2][2];
; #pragma unroll
;             for (int h = 0; h < 2; ++h)
; #pragma unroll
;                 for (int i = 0; i < 2; ++i) vo2[h][i] = (GATHER && last) ? voffN[h][i] : voffA[h][i];
;             PG8_LDB(B0, 0, 0); PG8_LDB(B1, 0, 1); PG8_SCHED; PG8_LDA(At, 0, 0); if (!rx) PG8_STAGE_A(PG8_SA(1, 1), a1, voffA, 1);
.LBB0_624:
	s_cmp_eq_u32 s16, 0
	s_cselect_b64 s[2:3], -1, 0
	s_and_b64 s[2:3], s[12:13], s[2:3]
	s_mov_b64 s[22:23], s[2:3]
	v_add_u32_e32 v4, 0x14000, v218
	v_add_u32_e32 v0, 0x10000, v218
	ds_read_b128 v[24:27], v0
	ds_read_b128 v[28:31], v0 offset:1024
	ds_read_b128 v[16:19], v0 offset:2048
	ds_read_b128 v[20:23], v0 offset:3072
	ds_read_b128 v[8:11], v4
	ds_read_b128 v[12:15], v4 offset:1024
	ds_read_b128 v[0:3], v4 offset:2048
	ds_read_b128 v[4:7], v4 offset:3072
	ds_read_b128 v[56:59], v219
	ds_read_b128 v[60:63], v219 offset:1024
	ds_read_b128 v[48:51], v219 offset:2048
	ds_read_b128 v[52:55], v219 offset:3072
	ds_read_b128 v[40:43], v219 offset:4096
	ds_read_b128 v[44:47], v219 offset:5120
	ds_read_b128 v[32:35], v219 offset:6144
	ds_read_b128 v[36:39], v219 offset:7168
	s_and_b64 vcc, exec, s[22:23]
	s_cbranch_vccz .LBB0_632
	s_waitcnt vmcnt(24)
	s_cbranch_execnz .LBB0_627

; #define PG8_STAGE_A(bufoff, gbase, VO, h) do { _Pragma("unroll") for (int _i = 0; _i < 2; ++_i) \
;         __builtin_amdgcn_global_load_lds((const unsigned*)((const char*)(gbase) + (VO)[h][_i]), (LAS unsigned*)(lds + (bufoff) + ldsw + _i * 8192), 16, 0, 0); } while (0)
; #define PG8_SCHED __builtin_amdgcn_sched_barrier(0)
;     ...
;             const bool last = (t == nt - 2); int rxi = (relax && t == 0) ? 1 : 0; asm volatile("" : "+v"(rxi)); const bool rx = __builtin_amdgcn_readfirstlane(rxi) != 0;
;             if constexpr (Epi::HAS_MID) { constexpr int SEGT = (F8 != 0) ? 8 : 16; if (t == SEGT || t == 2 * SEGT) { PG8_SCHED; E.mid(acc, cur, t / SEGT, wr, wc, fr, fq); PG8_SCHED; } }
;             const char* a1 = cA + (size_t)(t + 1) * kstep;
;             const char* a2 = last ? nA : cA + (size_t)(t + 2) * kstep; const char* b2 = last ? nB : cB + (size_t)(t + 2) * kstepB;
;             const char* a3 = a2 + kstep; const char* b3 = b2 + kstepB;
;             unsigned vo2[2][2];
; #pragma unroll
;             for (int h = 0; h < 2; ++h)
; #pragma unroll
;                 for (int i = 0; i < 2; ++i) vo2[h][i] = (GATHER && last) ? voffN[h][i] : voffA[h][i];
;             PG8_LDB(B0, 0, 0); PG8_LDB(B1, 0, 1); PG8_SCHED; PG8_LDA(At, 0, 0); if (!rx) PG8_STAGE_A(PG8_SA(1, 1), a1, voffA, 1);
.LBB0_795:
	s_cmp_eq_u32 s14, 0
	s_cselect_b64 s[2:3], -1, 0
	s_and_b64 s[2:3], s[10:11], s[2:3]
	s_mov_b64 s[20:21], s[2:3]
	v_add_u32_e32 v4, 0x14000, v219
	v_add_u32_e32 v0, 0x10000, v219
	ds_read_b128 v[24:27], v0
	ds_read_b128 v[28:31], v0 offset:1024
	ds_read_b128 v[16:19], v0 offset:2048
	ds_read_b128 v[20:23], v0 offset:3072
	ds_read_b128 v[8:11], v4
	ds_read_b128 v[12:15], v4 offset:1024
	ds_read_b128 v[0:3], v4 offset:2048
	ds_read_b128 v[4:7], v4 offset:3072
	ds_read_b128 v[56:59], v220
	ds_read_b128 v[60:63], v220 offset:1024
	ds_read_b128 v[48:51], v220 offset:2048
	ds_read_b128 v[52:55], v220 offset:3072
	ds_read_b128 v[40:43], v220 offset:4096
	ds_read_b128 v[44:47], v220 offset:5120
	ds_read_b128 v[32:35], v220 offset:6144
	ds_read_b128 v[36:39], v220 offset:7168
	s_and_b64 vcc, exec, s[20:21]
	s_cbranch_vccz .LBB0_803
	s_waitcnt vmcnt(24)
	s_cbranch_execnz .LBB0_798

; #define PG8_STAGE_A(bufoff, gbase, VO, h) do { _Pragma("unroll") for (int _i = 0; _i < 2; ++_i) \
;         __builtin_amdgcn_global_load_lds((const unsigned*)((const char*)(gbase) + (VO)[h][_i]), (LAS unsigned*)(lds + (bufoff) + ldsw + _i * 8192), 16, 0, 0); } while (0)
; #define PG8_SCHED __builtin_amdgcn_sched_barrier(0)
;     ...
;             const bool last = (t == nt - 2); int rxi = (relax && t == 0) ? 1 : 0; asm volatile("" : "+v"(rxi)); const bool rx = __builtin_amdgcn_readfirstlane(rxi) != 0;
;             if constexpr (Epi::HAS_MID) { constexpr int SEGT = (F8 != 0) ? 8 : 16; if (t == SEGT || t == 2 * SEGT) { PG8_SCHED; E.mid(acc, cur, t / SEGT, wr, wc, fr, fq); PG8_SCHED; } }
;             const char* a1 = cA + (size_t)(t + 1) * kstep;
;             const char* a2 = last ? nA : cA + (size_t)(t + 2) * kstep; const char* b2 = last ? nB : cB + (size_t)(t + 2) * kstepB;
;             const char* a3 = a2 + kstep; const char* b3 = b2 + kstepB;
;             unsigned vo2[2][2];
; #pragma unroll
;             for (int h = 0; h < 2; ++h)
; #pragma unroll
;                 for (int i = 0; i < 2; ++i) vo2[h][i] = (GATHER && last) ? voffN[h][i] : voffA[h][i];
;             PG8_LDB(B0, 0, 0); PG8_LDB(B1, 0, 1); PG8_SCHED; PG8_LDA(At, 0, 0); if (!rx) PG8_STAGE_A(PG8_SA(1, 1), a1, voffA, 1);
.LBB0_1299:
	s_cmp_eq_u32 s20, 0
	s_cselect_b64 s[4:5], -1, 0
	s_and_b64 s[4:5], s[18:19], s[4:5]
	s_mov_b64 s[26:27], s[4:5]
	v_add_u32_e32 v4, 0x14000, v207
	v_add_u32_e32 v0, 0x10000, v207
	ds_read_b128 v[24:27], v0
	ds_read_b128 v[28:31], v0 offset:1024
	ds_read_b128 v[16:19], v0 offset:2048
	ds_read_b128 v[20:23], v0 offset:3072
	ds_read_b128 v[8:11], v4
	ds_read_b128 v[12:15], v4 offset:1024
	ds_read_b128 v[0:3], v4 offset:2048
	ds_read_b128 v[4:7], v4 offset:3072
	ds_read_b128 v[56:59], v237
	ds_read_b128 v[60:63], v237 offset:1024
	ds_read_b128 v[48:51], v237 offset:2048
	ds_read_b128 v[52:55], v237 offset:3072
	ds_read_b128 v[40:43], v237 offset:4096
	ds_read_b128 v[44:47], v237 offset:5120
	ds_read_b128 v[32:35], v237 offset:6144
	ds_read_b128 v[36:39], v237 offset:7168
	s_and_b64 vcc, exec, s[26:27]
	s_cbranch_vccz .LBB0_1307
	s_waitcnt vmcnt(16)
	s_cbranch_execnz .LBB0_1302

; #define PG8_STAGE_A(bufoff, gbase, VO, h) do { _Pragma("unroll") for (int _i = 0; _i < 2; ++_i) \
;         __builtin_amdgcn_global_load_lds((const unsigned*)((const char*)(gbase) + (VO)[h][_i]), (LAS unsigned*)(lds + (bufoff) + ldsw + _i * 8192), 16, 0, 0); } while (0)
; #define PG8_SCHED __builtin_amdgcn_sched_barrier(0)
;     ...
;             const bool last = (t == nt - 2); int rxi = (relax && t == 0) ? 1 : 0; asm volatile("" : "+v"(rxi)); const bool rx = __builtin_amdgcn_readfirstlane(rxi) != 0;
;             if constexpr (Epi::HAS_MID) { constexpr int SEGT = (F8 != 0) ? 8 : 16; if (t == SEGT || t == 2 * SEGT) { PG8_SCHED; E.mid(acc, cur, t / SEGT, wr, wc, fr, fq); PG8_SCHED; } }
;             const char* a1 = cA + (size_t)(t + 1) * kstep;
;             const char* a2 = last ? nA : cA + (size_t)(t + 2) * kstep; const char* b2 = last ? nB : cB + (size_t)(t + 2) * kstepB;
;             const char* a3 = a2 + kstep; const char* b3 = b2 + kstepB;
;             unsigned vo2[2][2];
; #pragma unroll
;             for (int h = 0; h < 2; ++h)
; #pragma unroll
;                 for (int i = 0; i < 2; ++i) vo2[h][i] = (GATHER && last) ? voffN[h][i] : voffA[h][i];
;             PG8_LDB(B0, 0, 0); PG8_LDB(B1, 0, 1); PG8_SCHED; PG8_LDA(At, 0, 0); if (!rx) PG8_STAGE_A(PG8_SA(1, 1), a1, voffA, 1);
.LBB0_1411:
	s_and_b64 s[24:25], s[18:19], s[22:23]
	s_mov_b64 s[28:29], s[24:25]
	v_add_u32_e32 v4, 0x14000, v211
	v_add_u32_e32 v0, 0x10000, v211
	ds_read_b128 v[24:27], v0
	ds_read_b128 v[28:31], v0 offset:1024
	ds_read_b128 v[16:19], v0 offset:2048
	ds_read_b128 v[20:23], v0 offset:3072
	ds_read_b128 v[8:11], v4
	ds_read_b128 v[12:15], v4 offset:1024
	ds_read_b128 v[0:3], v4 offset:2048
	ds_read_b128 v[4:7], v4 offset:3072
	s_lshl_b32 s24, s5, 7
	s_add_u32 s24, s16, s24
	s_addc_u32 s25, s17, 0
	ds_read_b128 v[56:59], v212
	ds_read_b128 v[60:63], v212 offset:1024
	ds_read_b128 v[48:51], v212 offset:2048
	ds_read_b128 v[52:55], v212 offset:3072
	ds_read_b128 v[40:43], v212 offset:4096
	ds_read_b128 v[44:47], v212 offset:5120
	ds_read_b128 v[32:35], v212 offset:6144
	ds_read_b128 v[36:39], v212 offset:7168
	s_and_b64 vcc, exec, s[28:29]
	s_mov_b64 s[26:27], -1
	s_cbranch_vccz .LBB0_1413
	s_waitcnt vmcnt(16)
	s_mov_b64 s[26:27], 0
